# GEMM1 as two waves per SIMD: 128-col blocks, 32-col wave panels in 128 AGPRs, single A-fragment set refilled after use, 2 blocks per CU; w1t layout for 32-col waves
# speedup vs baseline: 1.1234x; 1.0057x over previous
.LBB1_32:
	s_lshr_b32 s0, s8, 6
	s_ff1_i32_b32 s1, s0
	s_and_b32 s2, s2, 0xff
	s_lshr_b32 s9, s2, s1
	v_lshrrev_b32_e32 v3, 6, v0
	v_and_b32_e32 v2, 63, v0
	s_add_i32 s0, s0, -1
	v_lshl_or_b32 v0, s9, 6, v3
	s_and_b32 s10, s2, s0
	v_mul_u32_u24_e32 v0, s8, v0
	s_lshl_b32 s0, s10, 8
	s_mov_b32 s1, 0
	v_lshlrev_b32_e32 v6, 2, v0
	v_mov_b32_e32 v7, 0
	v_lshl_add_u64 v[0:1], s[0:1], 0, v[6:7]
	v_lshlrev_b32_e32 v6, 2, v2
	v_lshl_add_u64 v[0:1], v[0:1], 0, v[6:7]
	s_movk_i32 s2, 0x104
	v_or_b32_e32 v4, -4, v3
	s_waitcnt lgkmcnt(0)
	v_lshl_add_u64 v[0:1], s[6:7], 0, v[0:1]
	s_lshl_b32 s0, s8, 4
	v_mad_u32_u24 v5, v3, s2, v6
	s_mov_b64 s[2:3], 0
	global_load_dword v6, v[0:1], off nt
	v_lshl_add_u64 v[0:1], v[0:1], 0, s[0:1]
	global_load_dword v7, v[0:1], off nt
	v_lshl_add_u64 v[0:1], v[0:1], 0, s[0:1]
	global_load_dword v8, v[0:1], off nt
	v_lshl_add_u64 v[0:1], v[0:1], 0, s[0:1]
	global_load_dword v9, v[0:1], off nt
	v_lshl_add_u64 v[0:1], v[0:1], 0, s[0:1]
	global_load_dword v10, v[0:1], off nt
	v_lshl_add_u64 v[0:1], v[0:1], 0, s[0:1]
	global_load_dword v11, v[0:1], off nt
	v_lshl_add_u64 v[0:1], v[0:1], 0, s[0:1]
	global_load_dword v12, v[0:1], off nt
	v_lshl_add_u64 v[0:1], v[0:1], 0, s[0:1]
	global_load_dword v13, v[0:1], off nt
	v_lshl_add_u64 v[0:1], v[0:1], 0, s[0:1]
	global_load_dword v14, v[0:1], off nt
	v_lshl_add_u64 v[0:1], v[0:1], 0, s[0:1]
	global_load_dword v15, v[0:1], off nt
	v_lshl_add_u64 v[0:1], v[0:1], 0, s[0:1]
	global_load_dword v16, v[0:1], off nt
	v_lshl_add_u64 v[0:1], v[0:1], 0, s[0:1]
	global_load_dword v17, v[0:1], off nt
	v_lshl_add_u64 v[0:1], v[0:1], 0, s[0:1]
	global_load_dword v18, v[0:1], off nt
	v_lshl_add_u64 v[0:1], v[0:1], 0, s[0:1]
	global_load_dword v19, v[0:1], off nt
	v_lshl_add_u64 v[0:1], v[0:1], 0, s[0:1]
	global_load_dword v20, v[0:1], off nt
	v_lshl_add_u64 v[0:1], v[0:1], 0, s[0:1]
	global_load_dword v21, v[0:1], off nt
	s_waitcnt vmcnt(0)
	ds_write_b32 v5, v6
	ds_write_b32 v5, v7 offset:1040
	ds_write_b32 v5, v8 offset:2080
	ds_write_b32 v5, v9 offset:3120
	ds_write_b32 v5, v10 offset:4160
	ds_write_b32 v5, v11 offset:5200
	ds_write_b32 v5, v12 offset:6240
	ds_write_b32 v5, v13 offset:7280
	ds_write_b32 v5, v14 offset:8320
	ds_write_b32 v5, v15 offset:9360
	ds_write_b32 v5, v16 offset:10400
	ds_write_b32 v5, v17 offset:11440
	ds_write_b32 v5, v18 offset:12480
	ds_write_b32 v5, v19 offset:13520
	ds_write_b32 v5, v20 offset:14560
	ds_write_b32 v5, v21 offset:15600
	v_lshlrev_b32_e32 v0, 8, v2
	v_lshl_or_b32 v0, v2, 2, v0
	v_lshl_add_u32 v4, v3, 2, v0
	s_waitcnt lgkmcnt(0)
	s_barrier
	ds_read2_b32 v[6:7], v4 offset1:4
	ds_read2_b32 v[8:9], v4 offset0:8 offset1:12
	ds_read2_b32 v[10:11], v4 offset0:16 offset1:20
	ds_read2_b32 v[12:13], v4 offset0:24 offset1:28
	ds_read2_b32 v[14:15], v4 offset0:32 offset1:36
	ds_read2_b32 v[16:17], v4 offset0:40 offset1:44
	ds_read2_b32 v[18:19], v4 offset0:48 offset1:52
	ds_read2_b32 v[20:21], v4 offset0:56 offset1:60
	v_bfe_u32 v0, v2, 3, 2
	v_lshlrev_b32_e32 v0, 8, v0
	v_and_b32_e32 v1, 7, v2
	v_lshl_or_b32 v0, v1, 1, v0
	v_lshl_or_b32 v0, v3, 4, v0
	v_lshrrev_b32_e32 v1, 5, v2
	s_waitcnt lgkmcnt(0)
	v_cvt_f16_f32_e32 v6, v6
	v_cvt_f16_f32_e32 v7, v7
	v_cvt_f16_f32_e32 v8, v8
	v_cvt_f16_f32_e32 v9, v9
	v_cvt_f16_f32_e32 v10, v10
	v_cvt_f16_f32_e32 v11, v11
	v_cvt_f16_f32_e32 v12, v12
	v_cvt_f16_f32_e32 v13, v13
	v_cvt_f16_f32_e32 v14, v14
	v_cvt_f16_f32_e32 v15, v15
	v_cvt_f16_f32_e32 v16, v16
	v_cvt_f16_f32_e32 v17, v17
	v_cvt_f16_f32_e32 v18, v18
	v_cvt_f16_f32_e32 v19, v19
	v_cvt_f16_f32_e32 v20, v20
	v_cvt_f16_f32_e32 v21, v21
	s_cmpk_eq_u32 s8, 0x200
	s_cbranch_scc1 .Lagg_w2t
	v_lshl_or_b32 v0, v1, 11, v0
	v_add_u32_e32 v1, 0x8000, v0
	s_lshl_b32 s0, s10, 16
	s_lshl_b32 s1, s9, 12
	s_add_i32 s0, s0, s1
	s_add_u32 s4, s4, s0
	s_addc_u32 s5, s5, 0
	global_store_short v0, v6, s[4:5]
	global_store_short v0, v7, s[4:5] offset:1024
	global_store_short v0, v8, s[4:5] offset:64
	global_store_short v0, v9, s[4:5] offset:1088
	global_store_short v0, v10, s[4:5] offset:128
	global_store_short v0, v11, s[4:5] offset:1152
	global_store_short v0, v12, s[4:5] offset:192
	global_store_short v0, v13, s[4:5] offset:1216
	global_store_short v1, v14, s[4:5]
	global_store_short v1, v15, s[4:5] offset:1024
	global_store_short v1, v16, s[4:5] offset:64
	global_store_short v1, v17, s[4:5] offset:1088
	global_store_short v1, v18, s[4:5] offset:128
	global_store_short v1, v19, s[4:5] offset:1152
	global_store_short v1, v20, s[4:5] offset:192
	global_store_short v1, v21, s[4:5] offset:1216
	s_endpgm

_Z6gemm_kILi1ELi2ELi2EEvPKDF16_S1_iiiPKfS1_PDF16_PfS4_:
	s_lshr_b32 s37, s2, 3
	s_and_b32 s36, s2, 7
	s_lshr_b32 s38, s37, 3
	s_lshl_b32 s36, s36, 3
	s_add_u32 s22, s36, s38
	s_and_b32 s21, s37, 7
	s_cmp_ge_u32 s22, 63
	s_cbranch_scc1 Lg1_exit
	s_load_dwordx4 s[4:7], s[0:1], 0x0
	s_load_dwordx4 s[8:11], s[0:1], 0x20
	s_load_dwordx4 s[12:15], s[0:1], 0x30
	s_load_dwordx2 s[16:17], s[0:1], 0x40
	v_lshrrev_b32_e32 v20, 6, v0
	v_and_b32_e32 v1, 63, v0
	v_readfirstlane_b32 s20, v20
	v_and_b32_e32 v2, 15, v0
	v_bfe_u32 v3, v0, 4, 2
	v_and_b32_e32 v16, 7, v2
	v_xor_b32_e32 v16, v16, v3
	v_lshlrev_b32_e32 v16, 4, v16
	v_lshl_or_b32 v4, v2, 7, v16
	v_lshrrev_b32_e32 v16, 3, v1
	v_and_b32_e32 v17, 7, v1
	v_xor_b32_e32 v17, v17, v16
	v_lshlrev_b32_e32 v17, 4, v17
	v_lshl_or_b32 v9, v16, 7, v17
	v_add_u32_e32 v10, 0x140000, v9
	s_mul_i32 s23, s22, 10
	s_sub_u32 s24, 625, s23
	s_min_u32 s24, s24, 10
	s_waitcnt lgkmcnt(0)
	s_mul_i32 s36, s20, 0x280000
	s_lshl_b32 s37, s23, 11
	s_add_u32 s36, s36, s37
	s_add_u32 s26, s4, s36
	s_addc_u32 s27, s5, 0
	s_mul_i32 s28, s20, 0x1000
	s_add_u32 s46, s28, 0x10000
	s_mov_b32 s47, s28
	s_mov_b32 s29, 0
	s_lshl_b32 s36, s21, 7
	s_lshl_b32 s37, s20, 5
	s_add_u32 s36, s36, s37
	v_lshlrev_b32_e32 v16, 3, v3
	v_add_u32_e32 v16, s36, v16
	v_lshlrev_b32_e32 v17, 2, v16
	global_load_dwordx4 v[32:35], v17, s[8:9] offset:0
	global_load_dwordx4 v[36:39], v17, s[8:9] offset:16
	v_mov_b32_e32 v12, 0x36b49f67
	s_mov_b32 s48, 0x384d0fec
	s_mov_b32 s49, 0x381f6607
	s_mov_b32 s50, 0x3b56cd72
	s_mov_b32 s51, 0x3cad2fe7
	s_mov_b32 s52, 0x3d4c41b4
	v_lshlrev_b32_e32 v18, 4, v3
	v_lshl_or_b32 v14, v2, 7, v18
	s_lshl_b32 s38, s21, 1
	s_lshr_b32 s39, s20, 1
	s_add_u32 s38, s38, s39
	s_mul_i32 s38, s38, 0x140000
	s_lshl_b32 s39, s23, 11
	s_add_u32 s38, s38, s39
	s_and_b32 s39, s20, 1
	s_lshl_b32 s39, s39, 6
	s_add_u32 s38, s38, s39
	s_add_u32 s30, s12, s38
	s_addc_u32 s31, s13, 0
	s_mov_b32 m0, s28
	s_add_u32 s28, s28, 0x4000
	s_cmp_ge_u32 s28, s46
	s_cselect_b32 s28, s47, s28
	global_load_lds_dwordx4 v9, s[26:27]
	global_load_lds_dwordx4 v9, s[26:27] offset:1024
	s_add_u32 m0, m0, 0x800
	s_nop 0
	global_load_lds_dwordx4 v10, s[26:27]
	global_load_lds_dwordx4 v10, s[26:27] offset:1024
	s_add_u32 s26, s26, 0x800
	s_addc_u32 s27, s27, 0
	s_mov_b32 m0, s28
	s_add_u32 s28, s28, 0x4000
	s_cmp_ge_u32 s28, s46
	s_cselect_b32 s28, s47, s28
	global_load_lds_dwordx4 v9, s[26:27]
	global_load_lds_dwordx4 v9, s[26:27] offset:1024
	s_add_u32 m0, m0, 0x800
	s_nop 0
	global_load_lds_dwordx4 v10, s[26:27]
	global_load_lds_dwordx4 v10, s[26:27] offset:1024
	s_add_u32 s26, s26, 0x800
	s_addc_u32 s27, s27, 0
	s_lshl_b32 s36, s21, 2
	s_add_u32 s36, s36, s20
	s_mul_i32 s36, s36, 0x8000
	v_lshlrev_b32_e32 v16, 4, v1
	v_add_u32_e32 v13, s36, v16
	global_load_dwordx4 a[0:3], v13, s[6:7] offset:0
	global_load_dwordx4 a[4:7], v13, s[6:7] offset:1024
	global_load_dwordx4 a[8:11], v13, s[6:7] offset:2048
	global_load_dwordx4 a[12:15], v13, s[6:7] offset:3072
	v_add_u32_e32 v13, 0x1000, v13
	global_load_dwordx4 a[16:19], v13, s[6:7] offset:0
	global_load_dwordx4 a[20:23], v13, s[6:7] offset:1024
	global_load_dwordx4 a[24:27], v13, s[6:7] offset:2048
	global_load_dwordx4 a[28:31], v13, s[6:7] offset:3072
	v_add_u32_e32 v13, 0x1000, v13
	global_load_dwordx4 a[32:35], v13, s[6:7] offset:0
	global_load_dwordx4 a[36:39], v13, s[6:7] offset:1024
	global_load_dwordx4 a[40:43], v13, s[6:7] offset:2048
	global_load_dwordx4 a[44:47], v13, s[6:7] offset:3072
	v_add_u32_e32 v13, 0x1000, v13
	global_load_dwordx4 a[48:51], v13, s[6:7] offset:0
	global_load_dwordx4 a[52:55], v13, s[6:7] offset:1024
	global_load_dwordx4 a[56:59], v13, s[6:7] offset:2048
	global_load_dwordx4 a[60:63], v13, s[6:7] offset:3072
	v_add_u32_e32 v13, 0x1000, v13
	global_load_dwordx4 a[64:67], v13, s[6:7] offset:0
	global_load_dwordx4 a[68:71], v13, s[6:7] offset:1024
	global_load_dwordx4 a[72:75], v13, s[6:7] offset:2048
	global_load_dwordx4 a[76:79], v13, s[6:7] offset:3072
	v_add_u32_e32 v13, 0x1000, v13
	global_load_dwordx4 a[80:83], v13, s[6:7] offset:0
	global_load_dwordx4 a[84:87], v13, s[6:7] offset:1024
	global_load_dwordx4 a[88:91], v13, s[6:7] offset:2048
	global_load_dwordx4 a[92:95], v13, s[6:7] offset:3072
	v_add_u32_e32 v13, 0x1000, v13
	global_load_dwordx4 a[96:99], v13, s[6:7] offset:0
	global_load_dwordx4 a[100:103], v13, s[6:7] offset:1024
	global_load_dwordx4 a[104:107], v13, s[6:7] offset:2048
	global_load_dwordx4 a[108:111], v13, s[6:7] offset:3072
	v_add_u32_e32 v13, 0x1000, v13
	global_load_dwordx4 a[112:115], v13, s[6:7] offset:0
	global_load_dwordx4 a[116:119], v13, s[6:7] offset:1024
	global_load_dwordx4 a[120:123], v13, s[6:7] offset:2048
	global_load_dwordx4 a[124:127], v13, s[6:7] offset:3072
	s_mov_b32 m0, s28
	s_add_u32 s28, s28, 0x4000
	s_cmp_ge_u32 s28, s46
	s_cselect_b32 s28, s47, s28
	global_load_lds_dwordx4 v9, s[26:27]
	global_load_lds_dwordx4 v9, s[26:27] offset:1024
	s_add_u32 m0, m0, 0x800
	s_nop 0
	global_load_lds_dwordx4 v10, s[26:27]
	global_load_lds_dwordx4 v10, s[26:27] offset:1024
	s_add_u32 s26, s26, 0x800
	s_addc_u32 s27, s27, 0
	s_waitcnt vmcnt(36)
	s_barrier
	v_add_u32_e32 v5, s29, v4
	v_xor_b32_e32 v6, 64, v5
	s_add_u32 s29, s29, 0x4000
	s_cmp_ge_u32 s29, 0x10000
	s_cselect_b32 s29, 0, s29
	ds_read_b128 v[64:67], v5 offset:0
	ds_read_b128 v[68:71], v6 offset:0
	ds_read_b128 v[72:75], v5 offset:2048
	ds_read_b128 v[76:79], v6 offset:2048
	ds_read_b128 v[80:83], v5 offset:4096
	ds_read_b128 v[84:87], v6 offset:4096
	ds_read_b128 v[88:91], v5 offset:6144
	ds_read_b128 v[92:95], v6 offset:6144
	ds_read_b128 v[96:99], v5 offset:8192
	ds_read_b128 v[100:103], v6 offset:8192
	ds_read_b128 v[104:107], v5 offset:10240
	ds_read_b128 v[108:111], v6 offset:10240
	ds_read_b128 v[112:115], v5 offset:12288
	ds_read_b128 v[116:119], v6 offset:12288
	ds_read_b128 v[120:123], v5 offset:14336
	ds_read_b128 v[124:127], v6 offset:14336
	v_add_u32_e32 v7, s29, v4
	v_xor_b32_e32 v8, 64, v7
	s_add_u32 s29, s29, 0x4000
	s_cmp_ge_u32 s29, 0x10000
	s_cselect_b32 s29, 0, s29
	s_mov_b32 m0, s28
	s_add_u32 s28, s28, 0x4000
	s_cmp_ge_u32 s28, s46
	s_cselect_b32 s28, s47, s28
	global_load_lds_dwordx4 v9, s[26:27]
	global_load_lds_dwordx4 v9, s[26:27] offset:1024
	s_add_u32 m0, m0, 0x800
	s_nop 0
	global_load_lds_dwordx4 v10, s[26:27]
	global_load_lds_dwordx4 v10, s[26:27] offset:1024
	s_add_u32 s26, s26, 0x800
	s_addc_u32 s27, s27, 0
	s_waitcnt vmcnt(38) lgkmcnt(15)
	v_mfma_f32_16x16x32_f16 v[40:43], a[0:3], v[64:67], v[32:35]
	v_mfma_f32_16x16x32_f16 v[44:47], a[4:7], v[64:67], v[36:39]
	ds_read_b128 v[64:67], v7 offset:0
	s_waitcnt vmcnt(36) lgkmcnt(15)
	v_mfma_f32_16x16x32_f16 v[40:43], a[8:11], v[68:71], v[40:43]
	v_mfma_f32_16x16x32_f16 v[44:47], a[12:15], v[68:71], v[44:47]
	ds_read_b128 v[68:71], v8 offset:0
	s_waitcnt vmcnt(34) lgkmcnt(15)
	v_mfma_f32_16x16x32_f16 v[40:43], a[16:19], v[72:75], v[40:43]
	v_mfma_f32_16x16x32_f16 v[44:47], a[20:23], v[72:75], v[44:47]
	ds_read_b128 v[72:75], v7 offset:2048
	s_waitcnt vmcnt(32) lgkmcnt(15)
	v_mfma_f32_16x16x32_f16 v[40:43], a[24:27], v[76:79], v[40:43]
	v_mfma_f32_16x16x32_f16 v[44:47], a[28:31], v[76:79], v[44:47]
	ds_read_b128 v[76:79], v8 offset:2048
	s_waitcnt vmcnt(30) lgkmcnt(15)
	v_mfma_f32_16x16x32_f16 v[40:43], a[32:35], v[80:83], v[40:43]
	v_mfma_f32_16x16x32_f16 v[44:47], a[36:39], v[80:83], v[44:47]
	ds_read_b128 v[80:83], v7 offset:4096
	s_waitcnt vmcnt(28) lgkmcnt(15)
	v_mfma_f32_16x16x32_f16 v[40:43], a[40:43], v[84:87], v[40:43]
	v_mfma_f32_16x16x32_f16 v[44:47], a[44:47], v[84:87], v[44:47]
	ds_read_b128 v[84:87], v8 offset:4096
	s_waitcnt vmcnt(26) lgkmcnt(15)
	v_mfma_f32_16x16x32_f16 v[40:43], a[48:51], v[88:91], v[40:43]
	v_mfma_f32_16x16x32_f16 v[44:47], a[52:55], v[88:91], v[44:47]
	ds_read_b128 v[88:91], v7 offset:6144
	s_waitcnt vmcnt(24) lgkmcnt(15)
	v_mfma_f32_16x16x32_f16 v[40:43], a[56:59], v[92:95], v[40:43]
	v_mfma_f32_16x16x32_f16 v[44:47], a[60:63], v[92:95], v[44:47]
	ds_read_b128 v[92:95], v8 offset:6144
	s_waitcnt vmcnt(22) lgkmcnt(15)
	v_mfma_f32_16x16x32_f16 v[40:43], a[64:67], v[96:99], v[40:43]
	v_mfma_f32_16x16x32_f16 v[44:47], a[68:71], v[96:99], v[44:47]
	ds_read_b128 v[96:99], v7 offset:8192
	s_waitcnt vmcnt(20) lgkmcnt(15)
	v_mfma_f32_16x16x32_f16 v[40:43], a[72:75], v[100:103], v[40:43]
	v_mfma_f32_16x16x32_f16 v[44:47], a[76:79], v[100:103], v[44:47]
	ds_read_b128 v[100:103], v8 offset:8192
	s_waitcnt vmcnt(18) lgkmcnt(15)
	v_mfma_f32_16x16x32_f16 v[40:43], a[80:83], v[104:107], v[40:43]
	v_mfma_f32_16x16x32_f16 v[44:47], a[84:87], v[104:107], v[44:47]
	ds_read_b128 v[104:107], v7 offset:10240
	s_waitcnt vmcnt(16) lgkmcnt(15)
	v_mfma_f32_16x16x32_f16 v[40:43], a[88:91], v[108:111], v[40:43]
	v_mfma_f32_16x16x32_f16 v[44:47], a[92:95], v[108:111], v[44:47]
	ds_read_b128 v[108:111], v8 offset:10240
	s_waitcnt vmcnt(14) lgkmcnt(15)
	v_mfma_f32_16x16x32_f16 v[40:43], a[96:99], v[112:115], v[40:43]
	v_mfma_f32_16x16x32_f16 v[44:47], a[100:103], v[112:115], v[44:47]
	ds_read_b128 v[112:115], v7 offset:12288
	s_waitcnt vmcnt(12) lgkmcnt(15)
	v_mfma_f32_16x16x32_f16 v[40:43], a[104:107], v[116:119], v[40:43]
	v_mfma_f32_16x16x32_f16 v[44:47], a[108:111], v[116:119], v[44:47]
	ds_read_b128 v[116:119], v8 offset:12288
	s_waitcnt vmcnt(10) lgkmcnt(15)
	v_mfma_f32_16x16x32_f16 v[40:43], a[112:115], v[120:123], v[40:43]
	v_mfma_f32_16x16x32_f16 v[44:47], a[116:119], v[120:123], v[44:47]
	ds_read_b128 v[120:123], v7 offset:14336
	s_waitcnt vmcnt(8) lgkmcnt(15)
	v_mfma_f32_16x16x32_f16 v[40:43], a[120:123], v[124:127], v[40:43]
	v_mfma_f32_16x16x32_f16 v[44:47], a[124:127], v[124:127], v[44:47]
	ds_read_b128 v[124:127], v8 offset:14336
Lg1_loop:
	s_waitcnt vmcnt(4)
	s_barrier
	v_add_u32_e32 v5, s29, v4
	v_xor_b32_e32 v6, 64, v5
	s_add_u32 s29, s29, 0x4000
	s_cmp_ge_u32 s29, 0x10000
	s_cselect_b32 s29, 0, s29
	s_waitcnt lgkmcnt(15)
	v_mfma_f32_16x16x32_f16 v[48:51], a[0:3], v[64:67], v[32:35]
	v_mfma_f32_16x16x32_f16 v[52:55], a[4:7], v[64:67], v[36:39]
	ds_read_b128 v[64:67], v5 offset:0
	v_fma_f32 v16, |v40|, v12, s48
	v_fma_f32 v16, |v40|, v16, s49
	v_fma_f32 v16, |v40|, v16, s50
	v_fma_f32 v16, |v40|, v16, s51
	v_fma_f32 v16, |v40|, v16, s52
	s_waitcnt lgkmcnt(15)
	v_mfma_f32_16x16x32_f16 v[48:51], a[8:11], v[68:71], v[48:51]
	v_fma_f32 v16, |v40|, v16, 1.0
	v_mul_f32_e32 v16, v16, v16
	v_mul_f32_e32 v16, v16, v16
	v_mul_f32_e32 v16, v16, v16
	v_mfma_f32_16x16x32_f16 v[52:55], a[12:15], v[68:71], v[52:55]
	ds_read_b128 v[68:71], v6 offset:0
	v_mul_f32_e32 v16, v16, v16
	v_rcp_f32_e32 v16, v16
	v_max_f32_e32 v17, 0, v40
	v_mul_f32_e64 v18, |v40|, v16
	s_waitcnt lgkmcnt(15)
	v_mfma_f32_16x16x32_f16 v[48:51], a[16:19], v[72:75], v[48:51]
	v_fmamk_f32 v56, v18, 0xbf000000, v17
	v_fma_f32 v19, |v41|, v12, s48
	v_fma_f32 v19, |v41|, v19, s49
	v_fma_f32 v19, |v41|, v19, s50
	v_mfma_f32_16x16x32_f16 v[52:55], a[20:23], v[72:75], v[52:55]
	ds_read_b128 v[72:75], v5 offset:2048
	v_fma_f32 v19, |v41|, v19, s51
	v_fma_f32 v19, |v41|, v19, s52
	v_fma_f32 v19, |v41|, v19, 1.0
	v_mul_f32_e32 v19, v19, v19
	s_waitcnt lgkmcnt(15)
	v_mfma_f32_16x16x32_f16 v[48:51], a[24:27], v[76:79], v[48:51]
	v_mul_f32_e32 v19, v19, v19
	v_mul_f32_e32 v19, v19, v19
	v_mul_f32_e32 v19, v19, v19
	v_rcp_f32_e32 v19, v19
	v_max_f32_e32 v20, 0, v41
	v_mfma_f32_16x16x32_f16 v[52:55], a[28:31], v[76:79], v[52:55]
	ds_read_b128 v[76:79], v6 offset:2048
	v_mul_f32_e64 v21, |v41|, v19
	v_fmamk_f32 v57, v21, 0xbf000000, v20
	v_fma_f32 v22, |v42|, v12, s48
	v_fma_f32 v22, |v42|, v22, s49
	s_waitcnt lgkmcnt(15)
	v_mfma_f32_16x16x32_f16 v[48:51], a[32:35], v[80:83], v[48:51]
	s_mov_b32 m0, s28
	s_add_u32 s28, s28, 0x4000
	s_cmp_ge_u32 s28, s46
	s_cselect_b32 s28, s47, s28
	global_load_lds_dwordx4 v9, s[26:27]
	v_fma_f32 v22, |v42|, v22, s50
	v_fma_f32 v22, |v42|, v22, s51
	v_fma_f32 v22, |v42|, v22, s52
	v_fma_f32 v22, |v42|, v22, 1.0
	v_mfma_f32_16x16x32_f16 v[52:55], a[36:39], v[80:83], v[52:55]
	ds_read_b128 v[80:83], v5 offset:4096
	v_mul_f32_e32 v22, v22, v22
	v_mul_f32_e32 v22, v22, v22
	v_mul_f32_e32 v22, v22, v22
	v_mul_f32_e32 v22, v22, v22
	s_waitcnt lgkmcnt(15)
	v_mfma_f32_16x16x32_f16 v[48:51], a[40:43], v[84:87], v[48:51]
	v_rcp_f32_e32 v22, v22
	v_max_f32_e32 v23, 0, v42
	v_mul_f32_e64 v24, |v42|, v22
	v_fmamk_f32 v58, v24, 0xbf000000, v23
	v_mfma_f32_16x16x32_f16 v[52:55], a[44:47], v[84:87], v[52:55]
	ds_read_b128 v[84:87], v6 offset:4096
	v_fma_f32 v25, |v43|, v12, s48
	v_fma_f32 v25, |v43|, v25, s49
	v_fma_f32 v25, |v43|, v25, s50
	v_fma_f32 v25, |v43|, v25, s51
	s_waitcnt lgkmcnt(15)
	v_mfma_f32_16x16x32_f16 v[48:51], a[48:51], v[88:91], v[48:51]
	v_fma_f32 v25, |v43|, v25, s52
	v_fma_f32 v25, |v43|, v25, 1.0
	v_mul_f32_e32 v25, v25, v25
	v_mul_f32_e32 v25, v25, v25
	v_mul_f32_e32 v25, v25, v25
	v_mfma_f32_16x16x32_f16 v[52:55], a[52:55], v[88:91], v[52:55]
	ds_read_b128 v[88:91], v5 offset:6144
	v_mul_f32_e32 v25, v25, v25
	v_rcp_f32_e32 v25, v25
	v_max_f32_e32 v26, 0, v43
	v_mul_f32_e64 v27, |v43|, v25
	s_waitcnt lgkmcnt(15)
	v_mfma_f32_16x16x32_f16 v[48:51], a[56:59], v[92:95], v[48:51]
	global_load_lds_dwordx4 v9, s[26:27] offset:1024
	v_fmamk_f32 v59, v27, 0xbf000000, v26
	v_fma_f32 v16, |v44|, v12, s48
	v_fma_f32 v16, |v44|, v16, s49
	v_fma_f32 v16, |v44|, v16, s50
	v_mfma_f32_16x16x32_f16 v[52:55], a[60:63], v[92:95], v[52:55]
	ds_read_b128 v[92:95], v6 offset:6144
	v_fma_f32 v16, |v44|, v16, s51
	v_fma_f32 v16, |v44|, v16, s52
	v_fma_f32 v16, |v44|, v16, 1.0
	v_mul_f32_e32 v16, v16, v16
	s_waitcnt lgkmcnt(15)
	v_mfma_f32_16x16x32_f16 v[48:51], a[64:67], v[96:99], v[48:51]
	v_mul_f32_e32 v16, v16, v16
	v_mul_f32_e32 v16, v16, v16
	v_mul_f32_e32 v16, v16, v16
	v_rcp_f32_e32 v16, v16
	v_mfma_f32_16x16x32_f16 v[52:55], a[68:71], v[96:99], v[52:55]
	ds_read_b128 v[96:99], v5 offset:8192
	v_max_f32_e32 v17, 0, v44
	v_mul_f32_e64 v18, |v44|, v16
	v_fmamk_f32 v60, v18, 0xbf000000, v17
	v_fma_f32 v19, |v45|, v12, s48
	v_fma_f32 v19, |v45|, v19, s49
	s_waitcnt lgkmcnt(15)
	v_mfma_f32_16x16x32_f16 v[48:51], a[72:75], v[100:103], v[48:51]
	v_fma_f32 v19, |v45|, v19, s50
	v_fma_f32 v19, |v45|, v19, s51
	v_fma_f32 v19, |v45|, v19, s52
	v_fma_f32 v19, |v45|, v19, 1.0
	v_mfma_f32_16x16x32_f16 v[52:55], a[76:79], v[100:103], v[52:55]
	ds_read_b128 v[100:103], v6 offset:8192
	v_mul_f32_e32 v19, v19, v19
	v_mul_f32_e32 v19, v19, v19
	v_mul_f32_e32 v19, v19, v19
	v_mul_f32_e32 v19, v19, v19
	s_waitcnt lgkmcnt(15)
	v_mfma_f32_16x16x32_f16 v[48:51], a[80:83], v[104:107], v[48:51]
	v_rcp_f32_e32 v19, v19
	v_max_f32_e32 v20, 0, v45
	v_mul_f32_e64 v21, |v45|, v19
	v_fmamk_f32 v61, v21, 0xbf000000, v20
	v_mfma_f32_16x16x32_f16 v[52:55], a[84:87], v[104:107], v[52:55]
	ds_read_b128 v[104:107], v5 offset:10240
	s_add_u32 m0, m0, 0x800
	s_nop 0
	global_load_lds_dwordx4 v10, s[26:27]
	v_fma_f32 v22, |v46|, v12, s48
	v_fma_f32 v22, |v46|, v22, s49
	v_fma_f32 v22, |v46|, v22, s50
	v_fma_f32 v22, |v46|, v22, s51
	s_waitcnt lgkmcnt(15)
	v_mfma_f32_16x16x32_f16 v[48:51], a[88:91], v[108:111], v[48:51]
	v_fma_f32 v22, |v46|, v22, s52
	v_fma_f32 v22, |v46|, v22, 1.0
	v_mul_f32_e32 v22, v22, v22
	v_mul_f32_e32 v22, v22, v22
	v_mfma_f32_16x16x32_f16 v[52:55], a[92:95], v[108:111], v[52:55]
	ds_read_b128 v[108:111], v6 offset:10240
	v_mul_f32_e32 v22, v22, v22
	v_mul_f32_e32 v22, v22, v22
	v_rcp_f32_e32 v22, v22
	v_max_f32_e32 v23, 0, v46
	v_mul_f32_e64 v24, |v46|, v22
	s_waitcnt lgkmcnt(15)
	v_mfma_f32_16x16x32_f16 v[48:51], a[96:99], v[112:115], v[48:51]
	v_fmamk_f32 v62, v24, 0xbf000000, v23
	v_fma_f32 v25, |v47|, v12, s48
	v_fma_f32 v25, |v47|, v25, s49
	v_fma_f32 v25, |v47|, v25, s50
	v_mfma_f32_16x16x32_f16 v[52:55], a[100:103], v[112:115], v[52:55]
	ds_read_b128 v[112:115], v5 offset:12288
	v_fma_f32 v25, |v47|, v25, s51
	v_fma_f32 v25, |v47|, v25, s52
	v_fma_f32 v25, |v47|, v25, 1.0
	v_mul_f32_e32 v25, v25, v25
	s_waitcnt lgkmcnt(15)
	v_mfma_f32_16x16x32_f16 v[48:51], a[104:107], v[116:119], v[48:51]
	v_mul_f32_e32 v25, v25, v25
	v_mul_f32_e32 v25, v25, v25
	v_mul_f32_e32 v25, v25, v25
	v_rcp_f32_e32 v25, v25
	v_mfma_f32_16x16x32_f16 v[52:55], a[108:111], v[116:119], v[52:55]
	ds_read_b128 v[116:119], v6 offset:12288
	v_max_f32_e32 v26, 0, v47
	v_mul_f32_e64 v27, |v47|, v25
	v_fmamk_f32 v63, v27, 0xbf000000, v26
	v_cvt_pk_f16_f32 v56, v56, v57
	s_waitcnt lgkmcnt(15)
	v_mfma_f32_16x16x32_f16 v[48:51], a[112:115], v[120:123], v[48:51]
	global_load_lds_dwordx4 v10, s[26:27] offset:1024
	v_cvt_pk_f16_f32 v57, v58, v59
	v_cvt_pk_f16_f32 v58, v60, v61
	v_cvt_pk_f16_f32 v59, v62, v63
	global_store_dwordx4 v14, v[56:59], s[30:31]
	v_mfma_f32_16x16x32_f16 v[52:55], a[116:119], v[120:123], v[52:55]
	ds_read_b128 v[120:123], v5 offset:14336
	s_add_u32 s26, s26, 0x800
	s_addc_u32 s27, s27, 0
	s_add_u32 s30, s30, 0x800
	s_addc_u32 s31, s31, 0
	s_waitcnt lgkmcnt(15)
	v_mfma_f32_16x16x32_f16 v[48:51], a[120:123], v[124:127], v[48:51]
	v_mfma_f32_16x16x32_f16 v[52:55], a[124:127], v[124:127], v[52:55]
	ds_read_b128 v[124:127], v6 offset:14336
	s_sub_u32 s24, s24, 1
	s_cmp_le_u32 s24, 1
	s_cbranch_scc1 Lg1_exitA
	s_waitcnt vmcnt(4)
	s_barrier
	v_add_u32_e32 v7, s29, v4
	v_xor_b32_e32 v8, 64, v7
	s_add_u32 s29, s29, 0x4000
	s_cmp_ge_u32 s29, 0x10000
	s_cselect_b32 s29, 0, s29
	s_waitcnt lgkmcnt(15)
	v_mfma_f32_16x16x32_f16 v[40:43], a[0:3], v[64:67], v[32:35]
	v_mfma_f32_16x16x32_f16 v[44:47], a[4:7], v[64:67], v[36:39]
	ds_read_b128 v[64:67], v7 offset:0
	v_fma_f32 v16, |v48|, v12, s48
	v_fma_f32 v16, |v48|, v16, s49
	v_fma_f32 v16, |v48|, v16, s50
	v_fma_f32 v16, |v48|, v16, s51
	v_fma_f32 v16, |v48|, v16, s52
	s_waitcnt lgkmcnt(15)
	v_mfma_f32_16x16x32_f16 v[40:43], a[8:11], v[68:71], v[40:43]
	v_fma_f32 v16, |v48|, v16, 1.0
	v_mul_f32_e32 v16, v16, v16
	v_mul_f32_e32 v16, v16, v16
	v_mul_f32_e32 v16, v16, v16
	v_mfma_f32_16x16x32_f16 v[44:47], a[12:15], v[68:71], v[44:47]
	ds_read_b128 v[68:71], v8 offset:0
	v_mul_f32_e32 v16, v16, v16
	v_rcp_f32_e32 v16, v16
	v_max_f32_e32 v17, 0, v48
	v_mul_f32_e64 v18, |v48|, v16
	s_waitcnt lgkmcnt(15)
	v_mfma_f32_16x16x32_f16 v[40:43], a[16:19], v[72:75], v[40:43]
	v_fmamk_f32 v56, v18, 0xbf000000, v17
	v_fma_f32 v19, |v49|, v12, s48
	v_fma_f32 v19, |v49|, v19, s49
	v_fma_f32 v19, |v49|, v19, s50
	v_mfma_f32_16x16x32_f16 v[44:47], a[20:23], v[72:75], v[44:47]
	ds_read_b128 v[72:75], v7 offset:2048
	v_fma_f32 v19, |v49|, v19, s51
	v_fma_f32 v19, |v49|, v19, s52
	v_fma_f32 v19, |v49|, v19, 1.0
	v_mul_f32_e32 v19, v19, v19
	s_waitcnt lgkmcnt(15)
	v_mfma_f32_16x16x32_f16 v[40:43], a[24:27], v[76:79], v[40:43]
	v_mul_f32_e32 v19, v19, v19
	v_mul_f32_e32 v19, v19, v19
	v_mul_f32_e32 v19, v19, v19
	v_rcp_f32_e32 v19, v19
	v_max_f32_e32 v20, 0, v49
	v_mfma_f32_16x16x32_f16 v[44:47], a[28:31], v[76:79], v[44:47]
	ds_read_b128 v[76:79], v8 offset:2048
	v_mul_f32_e64 v21, |v49|, v19
	v_fmamk_f32 v57, v21, 0xbf000000, v20
	v_fma_f32 v22, |v50|, v12, s48
	v_fma_f32 v22, |v50|, v22, s49
	s_waitcnt lgkmcnt(15)
	v_mfma_f32_16x16x32_f16 v[40:43], a[32:35], v[80:83], v[40:43]
	s_mov_b32 m0, s28
	s_add_u32 s28, s28, 0x4000
	s_cmp_ge_u32 s28, s46
	s_cselect_b32 s28, s47, s28
	global_load_lds_dwordx4 v9, s[26:27]
	v_fma_f32 v22, |v50|, v22, s50
	v_fma_f32 v22, |v50|, v22, s51
	v_fma_f32 v22, |v50|, v22, s52
	v_fma_f32 v22, |v50|, v22, 1.0
	v_mfma_f32_16x16x32_f16 v[44:47], a[36:39], v[80:83], v[44:47]
	ds_read_b128 v[80:83], v7 offset:4096
	v_mul_f32_e32 v22, v22, v22
	v_mul_f32_e32 v22, v22, v22
	v_mul_f32_e32 v22, v22, v22
	v_mul_f32_e32 v22, v22, v22
	s_waitcnt lgkmcnt(15)
	v_mfma_f32_16x16x32_f16 v[40:43], a[40:43], v[84:87], v[40:43]
	v_rcp_f32_e32 v22, v22
	v_max_f32_e32 v23, 0, v50
	v_mul_f32_e64 v24, |v50|, v22
	v_fmamk_f32 v58, v24, 0xbf000000, v23
	v_mfma_f32_16x16x32_f16 v[44:47], a[44:47], v[84:87], v[44:47]
	ds_read_b128 v[84:87], v8 offset:4096
	v_fma_f32 v25, |v51|, v12, s48
	v_fma_f32 v25, |v51|, v25, s49
	v_fma_f32 v25, |v51|, v25, s50
	v_fma_f32 v25, |v51|, v25, s51
	s_waitcnt lgkmcnt(15)
	v_mfma_f32_16x16x32_f16 v[40:43], a[48:51], v[88:91], v[40:43]
	v_fma_f32 v25, |v51|, v25, s52
	v_fma_f32 v25, |v51|, v25, 1.0
	v_mul_f32_e32 v25, v25, v25
	v_mul_f32_e32 v25, v25, v25
	v_mul_f32_e32 v25, v25, v25
	v_mfma_f32_16x16x32_f16 v[44:47], a[52:55], v[88:91], v[44:47]
	ds_read_b128 v[88:91], v7 offset:6144
	v_mul_f32_e32 v25, v25, v25
	v_rcp_f32_e32 v25, v25
	v_max_f32_e32 v26, 0, v51
	v_mul_f32_e64 v27, |v51|, v25
	s_waitcnt lgkmcnt(15)
	v_mfma_f32_16x16x32_f16 v[40:43], a[56:59], v[92:95], v[40:43]
	global_load_lds_dwordx4 v9, s[26:27] offset:1024
	v_fmamk_f32 v59, v27, 0xbf000000, v26
	v_fma_f32 v16, |v52|, v12, s48
	v_fma_f32 v16, |v52|, v16, s49
	v_fma_f32 v16, |v52|, v16, s50
	v_mfma_f32_16x16x32_f16 v[44:47], a[60:63], v[92:95], v[44:47]
	ds_read_b128 v[92:95], v8 offset:6144
	v_fma_f32 v16, |v52|, v16, s51
	v_fma_f32 v16, |v52|, v16, s52
	v_fma_f32 v16, |v52|, v16, 1.0
	v_mul_f32_e32 v16, v16, v16
	s_waitcnt lgkmcnt(15)
	v_mfma_f32_16x16x32_f16 v[40:43], a[64:67], v[96:99], v[40:43]
	v_mul_f32_e32 v16, v16, v16
	v_mul_f32_e32 v16, v16, v16
	v_mul_f32_e32 v16, v16, v16
	v_rcp_f32_e32 v16, v16
	v_mfma_f32_16x16x32_f16 v[44:47], a[68:71], v[96:99], v[44:47]
	ds_read_b128 v[96:99], v7 offset:8192
	v_max_f32_e32 v17, 0, v52
	v_mul_f32_e64 v18, |v52|, v16
	v_fmamk_f32 v60, v18, 0xbf000000, v17
	v_fma_f32 v19, |v53|, v12, s48
	v_fma_f32 v19, |v53|, v19, s49
	s_waitcnt lgkmcnt(15)
	v_mfma_f32_16x16x32_f16 v[40:43], a[72:75], v[100:103], v[40:43]
	v_fma_f32 v19, |v53|, v19, s50
	v_fma_f32 v19, |v53|, v19, s51
	v_fma_f32 v19, |v53|, v19, s52
	v_fma_f32 v19, |v53|, v19, 1.0
	v_mfma_f32_16x16x32_f16 v[44:47], a[76:79], v[100:103], v[44:47]
	ds_read_b128 v[100:103], v8 offset:8192
	v_mul_f32_e32 v19, v19, v19
	v_mul_f32_e32 v19, v19, v19
	v_mul_f32_e32 v19, v19, v19
	v_mul_f32_e32 v19, v19, v19
	s_waitcnt lgkmcnt(15)
	v_mfma_f32_16x16x32_f16 v[40:43], a[80:83], v[104:107], v[40:43]
	v_rcp_f32_e32 v19, v19
	v_max_f32_e32 v20, 0, v53
	v_mul_f32_e64 v21, |v53|, v19
	v_fmamk_f32 v61, v21, 0xbf000000, v20
	v_mfma_f32_16x16x32_f16 v[44:47], a[84:87], v[104:107], v[44:47]
	ds_read_b128 v[104:107], v7 offset:10240
	s_add_u32 m0, m0, 0x800
	s_nop 0
	global_load_lds_dwordx4 v10, s[26:27]
	v_fma_f32 v22, |v54|, v12, s48
	v_fma_f32 v22, |v54|, v22, s49
	v_fma_f32 v22, |v54|, v22, s50
	v_fma_f32 v22, |v54|, v22, s51
	s_waitcnt lgkmcnt(15)
	v_mfma_f32_16x16x32_f16 v[40:43], a[88:91], v[108:111], v[40:43]
	v_fma_f32 v22, |v54|, v22, s52
	v_fma_f32 v22, |v54|, v22, 1.0
	v_mul_f32_e32 v22, v22, v22
	v_mul_f32_e32 v22, v22, v22
	v_mfma_f32_16x16x32_f16 v[44:47], a[92:95], v[108:111], v[44:47]
	ds_read_b128 v[108:111], v8 offset:10240
	v_mul_f32_e32 v22, v22, v22
	v_mul_f32_e32 v22, v22, v22
	v_rcp_f32_e32 v22, v22
	v_max_f32_e32 v23, 0, v54
	v_mul_f32_e64 v24, |v54|, v22
	s_waitcnt lgkmcnt(15)
	v_mfma_f32_16x16x32_f16 v[40:43], a[96:99], v[112:115], v[40:43]
	v_fmamk_f32 v62, v24, 0xbf000000, v23
	v_fma_f32 v25, |v55|, v12, s48
	v_fma_f32 v25, |v55|, v25, s49
	v_fma_f32 v25, |v55|, v25, s50
	v_mfma_f32_16x16x32_f16 v[44:47], a[100:103], v[112:115], v[44:47]
	ds_read_b128 v[112:115], v7 offset:12288
	v_fma_f32 v25, |v55|, v25, s51
	v_fma_f32 v25, |v55|, v25, s52
	v_fma_f32 v25, |v55|, v25, 1.0
	v_mul_f32_e32 v25, v25, v25
	s_waitcnt lgkmcnt(15)
	v_mfma_f32_16x16x32_f16 v[40:43], a[104:107], v[116:119], v[40:43]
	v_mul_f32_e32 v25, v25, v25
	v_mul_f32_e32 v25, v25, v25
	v_mul_f32_e32 v25, v25, v25
	v_rcp_f32_e32 v25, v25
	v_mfma_f32_16x16x32_f16 v[44:47], a[108:111], v[116:119], v[44:47]
	ds_read_b128 v[116:119], v8 offset:12288
	v_max_f32_e32 v26, 0, v55
	v_mul_f32_e64 v27, |v55|, v25
	v_fmamk_f32 v63, v27, 0xbf000000, v26
	v_cvt_pk_f16_f32 v56, v56, v57
	s_waitcnt lgkmcnt(15)
	v_mfma_f32_16x16x32_f16 v[40:43], a[112:115], v[120:123], v[40:43]
	global_load_lds_dwordx4 v10, s[26:27] offset:1024
	v_cvt_pk_f16_f32 v57, v58, v59
	v_cvt_pk_f16_f32 v58, v60, v61
	v_cvt_pk_f16_f32 v59, v62, v63
	global_store_dwordx4 v14, v[56:59], s[30:31]
	v_mfma_f32_16x16x32_f16 v[44:47], a[116:119], v[120:123], v[44:47]
	ds_read_b128 v[120:123], v7 offset:14336
	s_add_u32 s26, s26, 0x800
	s_addc_u32 s27, s27, 0
	s_add_u32 s30, s30, 0x800
	s_addc_u32 s31, s31, 0
	s_waitcnt lgkmcnt(15)
	v_mfma_f32_16x16x32_f16 v[40:43], a[120:123], v[124:127], v[40:43]
	v_mfma_f32_16x16x32_f16 v[44:47], a[124:127], v[124:127], v[44:47]
	ds_read_b128 v[124:127], v8 offset:14336
	s_sub_u32 s24, s24, 1
	s_cmp_le_u32 s24, 1
	s_cbranch_scc0 Lg1_loop
	s_nop 7
	s_nop 7
	v_fma_f32 v16, |v40|, v12, s48
	v_fma_f32 v16, |v40|, v16, s49
	v_fma_f32 v16, |v40|, v16, s50
	v_fma_f32 v16, |v40|, v16, s51
	v_fma_f32 v16, |v40|, v16, s52
	v_fma_f32 v16, |v40|, v16, 1.0
	v_mul_f32_e32 v16, v16, v16
	v_mul_f32_e32 v16, v16, v16
	v_mul_f32_e32 v16, v16, v16
	v_mul_f32_e32 v16, v16, v16
	v_rcp_f32_e32 v16, v16
	v_max_f32_e32 v17, 0, v40
	v_mul_f32_e64 v18, |v40|, v16
	v_fmamk_f32 v56, v18, 0xbf000000, v17
	v_fma_f32 v19, |v41|, v12, s48
	v_fma_f32 v19, |v41|, v19, s49
	v_fma_f32 v19, |v41|, v19, s50
	v_fma_f32 v19, |v41|, v19, s51
	v_fma_f32 v19, |v41|, v19, s52
	v_fma_f32 v19, |v41|, v19, 1.0
	v_mul_f32_e32 v19, v19, v19
	v_mul_f32_e32 v19, v19, v19
	v_mul_f32_e32 v19, v19, v19
	v_mul_f32_e32 v19, v19, v19
	v_rcp_f32_e32 v19, v19
	v_max_f32_e32 v20, 0, v41
	v_mul_f32_e64 v21, |v41|, v19
	v_fmamk_f32 v57, v21, 0xbf000000, v20
	v_fma_f32 v22, |v42|, v12, s48
	v_fma_f32 v22, |v42|, v22, s49
	v_fma_f32 v22, |v42|, v22, s50
	v_fma_f32 v22, |v42|, v22, s51
	v_fma_f32 v22, |v42|, v22, s52
	v_fma_f32 v22, |v42|, v22, 1.0
	v_mul_f32_e32 v22, v22, v22
	v_mul_f32_e32 v22, v22, v22
	v_mul_f32_e32 v22, v22, v22
	v_mul_f32_e32 v22, v22, v22
	v_rcp_f32_e32 v22, v22
	v_max_f32_e32 v23, 0, v42
	v_mul_f32_e64 v24, |v42|, v22
	v_fmamk_f32 v58, v24, 0xbf000000, v23
	v_fma_f32 v25, |v43|, v12, s48
	v_fma_f32 v25, |v43|, v25, s49
	v_fma_f32 v25, |v43|, v25, s50
	v_fma_f32 v25, |v43|, v25, s51
	v_fma_f32 v25, |v43|, v25, s52
	v_fma_f32 v25, |v43|, v25, 1.0
	v_mul_f32_e32 v25, v25, v25
	v_mul_f32_e32 v25, v25, v25
	v_mul_f32_e32 v25, v25, v25
	v_mul_f32_e32 v25, v25, v25
	v_rcp_f32_e32 v25, v25
	v_max_f32_e32 v26, 0, v43
	v_mul_f32_e64 v27, |v43|, v25
	v_fmamk_f32 v59, v27, 0xbf000000, v26
	v_fma_f32 v16, |v44|, v12, s48
	v_fma_f32 v16, |v44|, v16, s49
	v_fma_f32 v16, |v44|, v16, s50
	v_fma_f32 v16, |v44|, v16, s51
	v_fma_f32 v16, |v44|, v16, s52
	v_fma_f32 v16, |v44|, v16, 1.0
	v_mul_f32_e32 v16, v16, v16
	v_mul_f32_e32 v16, v16, v16
	v_mul_f32_e32 v16, v16, v16
	v_mul_f32_e32 v16, v16, v16
	v_rcp_f32_e32 v16, v16
	v_max_f32_e32 v17, 0, v44
	v_mul_f32_e64 v18, |v44|, v16
	v_fmamk_f32 v60, v18, 0xbf000000, v17
	v_fma_f32 v19, |v45|, v12, s48
	v_fma_f32 v19, |v45|, v19, s49
	v_fma_f32 v19, |v45|, v19, s50
	v_fma_f32 v19, |v45|, v19, s51
	v_fma_f32 v19, |v45|, v19, s52
	v_fma_f32 v19, |v45|, v19, 1.0
	v_mul_f32_e32 v19, v19, v19
	v_mul_f32_e32 v19, v19, v19
	v_mul_f32_e32 v19, v19, v19
	v_mul_f32_e32 v19, v19, v19
	v_rcp_f32_e32 v19, v19
	v_max_f32_e32 v20, 0, v45
	v_mul_f32_e64 v21, |v45|, v19
	v_fmamk_f32 v61, v21, 0xbf000000, v20
	v_fma_f32 v22, |v46|, v12, s48
	v_fma_f32 v22, |v46|, v22, s49
	v_fma_f32 v22, |v46|, v22, s50
	v_fma_f32 v22, |v46|, v22, s51
	v_fma_f32 v22, |v46|, v22, s52
	v_fma_f32 v22, |v46|, v22, 1.0
	v_mul_f32_e32 v22, v22, v22
	v_mul_f32_e32 v22, v22, v22
	v_mul_f32_e32 v22, v22, v22
	v_mul_f32_e32 v22, v22, v22
	v_rcp_f32_e32 v22, v22
	v_max_f32_e32 v23, 0, v46
	v_mul_f32_e64 v24, |v46|, v22
	v_fmamk_f32 v62, v24, 0xbf000000, v23
	v_fma_f32 v25, |v47|, v12, s48
	v_fma_f32 v25, |v47|, v25, s49
	v_fma_f32 v25, |v47|, v25, s50
	v_fma_f32 v25, |v47|, v25, s51
	v_fma_f32 v25, |v47|, v25, s52
	v_fma_f32 v25, |v47|, v25, 1.0
	v_mul_f32_e32 v25, v25, v25
	v_mul_f32_e32 v25, v25, v25
	v_mul_f32_e32 v25, v25, v25
	v_mul_f32_e32 v25, v25, v25
	v_rcp_f32_e32 v25, v25
	v_max_f32_e32 v26, 0, v47
	v_mul_f32_e64 v27, |v47|, v25
	v_fmamk_f32 v63, v27, 0xbf000000, v26
	v_cvt_pk_f16_f32 v56, v56, v57
	v_cvt_pk_f16_f32 v57, v58, v59
	v_cvt_pk_f16_f32 v58, v60, v61
	v_cvt_pk_f16_f32 v59, v62, v63
	global_store_dwordx4 v14, v[56:59], s[30:31]
	s_add_u32 s30, s30, 0x800
	s_addc_u32 s31, s31, 0
	s_endpgm
Lg1_exitA:
	s_nop 7
	s_nop 7
	v_fma_f32 v16, |v48|, v12, s48
	v_fma_f32 v16, |v48|, v16, s49
	v_fma_f32 v16, |v48|, v16, s50
	v_fma_f32 v16, |v48|, v16, s51
	v_fma_f32 v16, |v48|, v16, s52
	v_fma_f32 v16, |v48|, v16, 1.0
	v_mul_f32_e32 v16, v16, v16
	v_mul_f32_e32 v16, v16, v16
	v_mul_f32_e32 v16, v16, v16
	v_mul_f32_e32 v16, v16, v16
	v_rcp_f32_e32 v16, v16
	v_max_f32_e32 v17, 0, v48
	v_mul_f32_e64 v18, |v48|, v16
	v_fmamk_f32 v56, v18, 0xbf000000, v17
	v_fma_f32 v19, |v49|, v12, s48
	v_fma_f32 v19, |v49|, v19, s49
	v_fma_f32 v19, |v49|, v19, s50
	v_fma_f32 v19, |v49|, v19, s51
	v_fma_f32 v19, |v49|, v19, s52
	v_fma_f32 v19, |v49|, v19, 1.0
	v_mul_f32_e32 v19, v19, v19
	v_mul_f32_e32 v19, v19, v19
	v_mul_f32_e32 v19, v19, v19
	v_mul_f32_e32 v19, v19, v19
	v_rcp_f32_e32 v19, v19
	v_max_f32_e32 v20, 0, v49
	v_mul_f32_e64 v21, |v49|, v19
	v_fmamk_f32 v57, v21, 0xbf000000, v20
	v_fma_f32 v22, |v50|, v12, s48
	v_fma_f32 v22, |v50|, v22, s49
	v_fma_f32 v22, |v50|, v22, s50
	v_fma_f32 v22, |v50|, v22, s51
	v_fma_f32 v22, |v50|, v22, s52
	v_fma_f32 v22, |v50|, v22, 1.0
	v_mul_f32_e32 v22, v22, v22
	v_mul_f32_e32 v22, v22, v22
	v_mul_f32_e32 v22, v22, v22
	v_mul_f32_e32 v22, v22, v22
	v_rcp_f32_e32 v22, v22
	v_max_f32_e32 v23, 0, v50
	v_mul_f32_e64 v24, |v50|, v22
	v_fmamk_f32 v58, v24, 0xbf000000, v23
	v_fma_f32 v25, |v51|, v12, s48
	v_fma_f32 v25, |v51|, v25, s49
	v_fma_f32 v25, |v51|, v25, s50
	v_fma_f32 v25, |v51|, v25, s51
	v_fma_f32 v25, |v51|, v25, s52
	v_fma_f32 v25, |v51|, v25, 1.0
	v_mul_f32_e32 v25, v25, v25
	v_mul_f32_e32 v25, v25, v25
	v_mul_f32_e32 v25, v25, v25
	v_mul_f32_e32 v25, v25, v25
	v_rcp_f32_e32 v25, v25
	v_max_f32_e32 v26, 0, v51
	v_mul_f32_e64 v27, |v51|, v25
	v_fmamk_f32 v59, v27, 0xbf000000, v26
	v_fma_f32 v16, |v52|, v12, s48
	v_fma_f32 v16, |v52|, v16, s49
	v_fma_f32 v16, |v52|, v16, s50
	v_fma_f32 v16, |v52|, v16, s51
	v_fma_f32 v16, |v52|, v16, s52
	v_fma_f32 v16, |v52|, v16, 1.0
	v_mul_f32_e32 v16, v16, v16
	v_mul_f32_e32 v16, v16, v16
	v_mul_f32_e32 v16, v16, v16
	v_mul_f32_e32 v16, v16, v16
	v_rcp_f32_e32 v16, v16
	v_max_f32_e32 v17, 0, v52
	v_mul_f32_e64 v18, |v52|, v16
	v_fmamk_f32 v60, v18, 0xbf000000, v17
	v_fma_f32 v19, |v53|, v12, s48
	v_fma_f32 v19, |v53|, v19, s49
	v_fma_f32 v19, |v53|, v19, s50
	v_fma_f32 v19, |v53|, v19, s51
	v_fma_f32 v19, |v53|, v19, s52
	v_fma_f32 v19, |v53|, v19, 1.0
	v_mul_f32_e32 v19, v19, v19
	v_mul_f32_e32 v19, v19, v19
	v_mul_f32_e32 v19, v19, v19
	v_mul_f32_e32 v19, v19, v19
	v_rcp_f32_e32 v19, v19
	v_max_f32_e32 v20, 0, v53
	v_mul_f32_e64 v21, |v53|, v19
	v_fmamk_f32 v61, v21, 0xbf000000, v20
	v_fma_f32 v22, |v54|, v12, s48
	v_fma_f32 v22, |v54|, v22, s49
	v_fma_f32 v22, |v54|, v22, s50
	v_fma_f32 v22, |v54|, v22, s51
	v_fma_f32 v22, |v54|, v22, s52
	v_fma_f32 v22, |v54|, v22, 1.0
	v_mul_f32_e32 v22, v22, v22
	v_mul_f32_e32 v22, v22, v22
	v_mul_f32_e32 v22, v22, v22
	v_mul_f32_e32 v22, v22, v22
	v_rcp_f32_e32 v22, v22
	v_max_f32_e32 v23, 0, v54
	v_mul_f32_e64 v24, |v54|, v22
	v_fmamk_f32 v62, v24, 0xbf000000, v23
	v_fma_f32 v25, |v55|, v12, s48
	v_fma_f32 v25, |v55|, v25, s49
	v_fma_f32 v25, |v55|, v25, s50
	v_fma_f32 v25, |v55|, v25, s51
	v_fma_f32 v25, |v55|, v25, s52
	v_fma_f32 v25, |v55|, v25, 1.0
	v_mul_f32_e32 v25, v25, v25
	v_mul_f32_e32 v25, v25, v25
	v_mul_f32_e32 v25, v25, v25
	v_mul_f32_e32 v25, v25, v25
	v_rcp_f32_e32 v25, v25
	v_max_f32_e32 v26, 0, v55
	v_mul_f32_e64 v27, |v55|, v25
	v_fmamk_f32 v63, v27, 0xbf000000, v26
	v_cvt_pk_f16_f32 v56, v56, v57
	v_cvt_pk_f16_f32 v57, v58, v59
	v_cvt_pk_f16_f32 v58, v60, v61
	v_cvt_pk_f16_f32 v59, v62, v63
	global_store_dwordx4 v14, v[56:59], s[30:31]
	s_add_u32 s30, s30, 0x800
	s_addc_u32 s31, s31, 0
	s_endpgm

	.amdhsa_kernel _Z6gemm_kILi1ELi2ELi2EEvPKDF16_S1_iiiPKfS1_PDF16_PfS4_
		.amdhsa_group_segment_fixed_size 65536
		.amdhsa_private_segment_fixed_size 0
		.amdhsa_kernarg_size 72
		.amdhsa_user_sgpr_count 2
		.amdhsa_user_sgpr_dispatch_ptr 0
		.amdhsa_user_sgpr_queue_ptr 0
		.amdhsa_user_sgpr_kernarg_segment_ptr 1
		.amdhsa_user_sgpr_dispatch_id 0
		.amdhsa_user_sgpr_kernarg_preload_length 0
		.amdhsa_user_sgpr_kernarg_preload_offset 0
		.amdhsa_user_sgpr_private_segment_size 0
		.amdhsa_uses_dynamic_stack 0
		.amdhsa_enable_private_segment 0
		.amdhsa_system_sgpr_workgroup_id_x 1
		.amdhsa_system_sgpr_workgroup_id_y 0
		.amdhsa_system_sgpr_workgroup_id_z 0
		.amdhsa_system_sgpr_workgroup_info 0
		.amdhsa_system_vgpr_workitem_id 0
		.amdhsa_next_free_vgpr 256
		.amdhsa_next_free_sgpr 56
		.amdhsa_accum_offset 128
		.amdhsa_reserve_vcc 1
		.amdhsa_float_round_mode_32 0
		.amdhsa_float_round_mode_16_64 0
		.amdhsa_float_denorm_mode_32 3
		.amdhsa_float_denorm_mode_16_64 3
		.amdhsa_dx10_clamp 1
		.amdhsa_ieee_mode 1
		.amdhsa_fp16_overflow 0
		.amdhsa_tg_split 0
		.amdhsa_exception_fp_ieee_invalid_op 0
		.amdhsa_exception_fp_denorm_src 0
		.amdhsa_exception_fp_ieee_div_zero 0
		.amdhsa_exception_fp_ieee_overflow 0
		.amdhsa_exception_fp_ieee_underflow 0
		.amdhsa_exception_fp_ieee_inexact 0
		.amdhsa_exception_int_div_zero 0
	.end_amdhsa_kernel

Lg2_exitA:
	s_nop 7
	s_nop 7
	s_waitcnt vmcnt(0)
	v_cvt_f32_f16_e32 v16, v88
	v_cvt_f32_f16_sdwa v17, v88 dst_sel:DWORD dst_unused:UNUSED_PAD src0_sel:WORD_1
	v_cvt_f32_f16_e32 v18, v89
	v_cvt_f32_f16_sdwa v19, v89 dst_sel:DWORD dst_unused:UNUSED_PAD src0_sel:WORD_1
	v_cvt_f32_f16_e32 v20, v90
	v_cvt_f32_f16_sdwa v21, v90 dst_sel:DWORD dst_unused:UNUSED_PAD src0_sel:WORD_1
	v_cvt_f32_f16_e32 v22, v91
	v_cvt_f32_f16_sdwa v23, v91 dst_sel:DWORD dst_unused:UNUSED_PAD src0_sel:WORD_1
	v_add_f32_e32 v16, v16, v64
	v_add_f32_e32 v17, v17, v65
	v_add_f32_e32 v18, v18, v66
	v_add_f32_e32 v19, v19, v67
	v_add_f32_e32 v20, v20, v68
	v_add_f32_e32 v21, v21, v69
	v_add_f32_e32 v22, v22, v70
	v_add_f32_e32 v23, v23, v71
	v_cvt_pk_f16_f32 v24, v16, v17
	v_cvt_pk_f16_f32 v25, v18, v19
	v_cvt_pk_f16_f32 v26, v20, v21
	v_cvt_pk_f16_f32 v27, v22, v23
	global_store_dwordx4 v14, v[24:27], s[30:31]
	s_add_u32 s30, s30, 0x4000
	s_addc_u32 s31, s31, 0
	s_endpgm

amdhsa.kernels:
  - .agpr_count:     0
    .args:
      - .actual_access:  read_only
        .address_space:  global
        .offset:         0
        .size:           8
        .value_kind:     global_buffer
      - .actual_access:  write_only
        .address_space:  global
        .offset:         8
        .size:           8
        .value_kind:     global_buffer
      - .actual_access:  read_only
        .address_space:  global
        .offset:         16
        .size:           8
        .value_kind:     global_buffer
      - .actual_access:  read_only
        .address_space:  global
        .offset:         24
        .size:           8
        .value_kind:     global_buffer
      - .actual_access:  read_only
        .address_space:  global
        .offset:         32
        .size:           8
        .value_kind:     global_buffer
      - .actual_access:  read_only
        .address_space:  global
        .offset:         40
        .size:           8
        .value_kind:     global_buffer
      - .actual_access:  write_only
        .address_space:  global
        .offset:         48
        .size:           8
        .value_kind:     global_buffer
      - .actual_access:  read_only
        .address_space:  global
        .offset:         56
        .size:           8
        .value_kind:     global_buffer
      - .actual_access:  read_only
        .address_space:  global
        .offset:         64
        .size:           8
        .value_kind:     global_buffer
      - .actual_access:  read_only
        .address_space:  global
        .offset:         72
        .size:           8
        .value_kind:     global_buffer
      - .actual_access:  read_only
        .address_space:  global
        .offset:         80
        .size:           8
        .value_kind:     global_buffer
      - .actual_access:  read_only
        .address_space:  global
        .offset:         88
        .size:           8
        .value_kind:     global_buffer
      - .actual_access:  write_only
        .address_space:  global
        .offset:         96
        .size:           8
        .value_kind:     global_buffer
      - .actual_access:  write_only
        .address_space:  global
        .offset:         104
        .size:           8
        .value_kind:     global_buffer
      - .actual_access:  write_only
        .address_space:  global
        .offset:         112
        .size:           8
        .value_kind:     global_buffer
    .group_segment_fixed_size: 51552
    .kernarg_segment_align: 8
    .kernarg_segment_size: 120
    .language:       OpenCL C
    .language_version:
      - 2
      - 0
    .max_flat_workgroup_size: 1024
    .name:           _Z6prep_kPKfPDF16_S0_S0_S0_S0_S1_S1_S1_PKiS3_S3_PiS4_S4_
    .private_segment_fixed_size: 0
    .sgpr_count:     106
    .sgpr_spill_count: 15
    .symbol:         _Z6prep_kPKfPDF16_S0_S0_S0_S0_S1_S1_S1_PKiS3_S3_PiS4_S4_.kd
    .uniform_work_group_size: 1
    .uses_dynamic_stack: false
    .vgpr_count:     48
    .vgpr_spill_count: 0
    .wavefront_size: 64
  - .agpr_count:     0
    .args:
      - .actual_access:  read_only
        .address_space:  global
        .offset:         0
        .size:           8
        .value_kind:     global_buffer
      - .actual_access:  read_only
        .address_space:  global
        .offset:         8
        .size:           8
        .value_kind:     global_buffer
      - .actual_access:  read_only
        .address_space:  global
        .offset:         16
        .size:           8
        .value_kind:     global_buffer
      - .actual_access:  read_only
        .address_space:  global
        .offset:         24
        .size:           8
        .value_kind:     global_buffer
      - .actual_access:  read_only
        .address_space:  global
        .offset:         32
        .size:           8
        .value_kind:     global_buffer
      - .actual_access:  read_only
        .address_space:  global
        .offset:         40
        .size:           8
        .value_kind:     global_buffer
      - .actual_access:  read_only
        .address_space:  global
        .offset:         48
        .size:           8
        .value_kind:     global_buffer
      - .actual_access:  read_only
        .address_space:  global
        .offset:         56
        .size:           8
        .value_kind:     global_buffer
      - .actual_access:  read_only
        .address_space:  global
        .offset:         64
        .size:           8
        .value_kind:     global_buffer
      - .actual_access:  write_only
        .address_space:  global
        .offset:         72
        .size:           8
        .value_kind:     global_buffer
      - .actual_access:  read_only
        .address_space:  global
        .offset:         80
        .size:           8
        .value_kind:     global_buffer
      - .actual_access:  read_only
        .address_space:  global
        .offset:         88
        .size:           8
        .value_kind:     global_buffer
      - .actual_access:  write_only
        .address_space:  global
        .offset:         96
        .size:           8
        .value_kind:     global_buffer
      - .actual_access:  write_only
        .address_space:  global
        .offset:         104
        .size:           8
        .value_kind:     global_buffer
    .group_segment_fixed_size: 16640
    .kernarg_segment_align: 8
    .kernarg_segment_size: 112
    .language:       OpenCL C
    .language_version:
      - 2
      - 0
    .max_flat_workgroup_size: 256
    .name:           _Z7agg_ln1PKDF16_S0_S0_PKiS2_S2_PKfS4_S4_PDF16_S4_S4_S5_S5_
    .private_segment_fixed_size: 0
    .sgpr_count:     45
    .sgpr_spill_count: 0
    .symbol:         _Z7agg_ln1PKDF16_S0_S0_PKiS2_S2_PKfS4_S4_PDF16_S4_S4_S5_S5_.kd
    .uniform_work_group_size: 1
    .uses_dynamic_stack: false
    .vgpr_count:     64
    .vgpr_spill_count: 0
    .wavefront_size: 64
  - .agpr_count:     0
    .args:
      - .actual_access:  read_only
        .address_space:  global
        .offset:         0
        .size:           8
        .value_kind:     global_buffer
      - .actual_access:  read_only
        .address_space:  global
        .offset:         8
        .size:           8
        .value_kind:     global_buffer
      - .actual_access:  read_only
        .address_space:  global
        .offset:         16
        .size:           8
        .value_kind:     global_buffer
      - .actual_access:  write_only
        .address_space:  global
        .offset:         24
        .size:           8
        .value_kind:     global_buffer
    .group_segment_fixed_size: 0
    .kernarg_segment_align: 8
    .kernarg_segment_size: 32
    .language:       OpenCL C
    .language_version:
      - 2
      - 0
    .max_flat_workgroup_size: 256
    .name:           _Z5ln2_kPKDF16_PKfS2_Pf
    .private_segment_fixed_size: 0
    .sgpr_count:     18
    .sgpr_spill_count: 0
    .symbol:         _Z5ln2_kPKDF16_PKfS2_Pf.kd
    .uniform_work_group_size: 1
    .uses_dynamic_stack: false
    .vgpr_count:     37
    .vgpr_spill_count: 0
    .wavefront_size: 64
  - .agpr_count:     256
    .args:
      - .address_space:  global
        .offset:         0
        .size:           8
        .value_kind:     global_buffer
      - .address_space:  global
        .offset:         8
        .size:           8
        .value_kind:     global_buffer
      - .offset:         16
        .size:           4
        .value_kind:     by_value
      - .offset:         20
        .size:           4
        .value_kind:     by_value
      - .offset:         24
        .size:           4
        .value_kind:     by_value
      - .actual_access:  read_only
        .address_space:  global
        .offset:         32
        .size:           8
        .value_kind:     global_buffer
      - .actual_access:  read_only
        .address_space:  global
        .offset:         40
        .size:           8
        .value_kind:     global_buffer
      - .actual_access:  write_only
        .address_space:  global
        .offset:         48
        .size:           8
        .value_kind:     global_buffer
      - .actual_access:  read_only
        .address_space:  global
        .offset:         56
        .size:           8
        .value_kind:     global_buffer
      - .actual_access:  write_only
        .address_space:  global
        .offset:         64
        .size:           8
        .value_kind:     global_buffer
    .group_segment_fixed_size: 81920
    .kernarg_segment_align: 8
    .kernarg_segment_size: 72
    .language:       OpenCL C
    .language_version:
      - 2
      - 0
    .max_flat_workgroup_size: 256
    .name:           _Z6gemm_kILi0ELi1ELi2EEvPKDF16_S1_iiiPKfS1_PDF16_PfS4_
    .private_segment_fixed_size: 0
    .sgpr_count:     70
    .sgpr_spill_count: 0
    .symbol:         _Z6gemm_kILi0ELi1ELi2EEvPKDF16_S1_iiiPKfS1_PDF16_PfS4_.kd
    .uniform_work_group_size: 1
    .uses_dynamic_stack: false
    .vgpr_count:     512
    .vgpr_spill_count: 0
    .wavefront_size: 64
  - .agpr_count:     128
    .args:
      - .address_space:  global
        .offset:         0
        .size:           8
        .value_kind:     global_buffer
      - .address_space:  global
        .offset:         8
        .size:           8
        .value_kind:     global_buffer
      - .offset:         16
        .size:           4
        .value_kind:     by_value
      - .offset:         20
        .size:           4
        .value_kind:     by_value
      - .offset:         24
        .size:           4
        .value_kind:     by_value
      - .actual_access:  read_only
        .address_space:  global
        .offset:         32
        .size:           8
        .value_kind:     global_buffer
      - .actual_access:  read_only
        .address_space:  global
        .offset:         40
        .size:           8
        .value_kind:     global_buffer
      - .actual_access:  write_only
        .address_space:  global
        .offset:         48
        .size:           8
        .value_kind:     global_buffer
      - .actual_access:  read_only
        .address_space:  global
        .offset:         56
        .size:           8
        .value_kind:     global_buffer
      - .actual_access:  read_only
        .address_space:  global
        .offset:         64
        .size:           8
        .value_kind:     global_buffer
    .group_segment_fixed_size: 65536
    .kernarg_segment_align: 8
    .kernarg_segment_size: 72
    .language:       OpenCL C
    .language_version:
      - 2
      - 0
    .max_flat_workgroup_size: 256
    .name:           _Z6gemm_kILi1ELi2ELi2EEvPKDF16_S1_iiiPKfS1_PDF16_PfS4_
    .private_segment_fixed_size: 0
    .sgpr_count:     62
    .sgpr_spill_count: 0
    .symbol:         _Z6gemm_kILi1ELi2ELi2EEvPKDF16_S1_iiiPKfS1_PDF16_PfS4_.kd
    .uniform_work_group_size: 1
    .uses_dynamic_stack: false
    .vgpr_count:     256
    .vgpr_spill_count: 0
    .wavefront_size: 64
  - .agpr_count:     256
    .args:
      - .address_space:  global
        .offset:         0
        .size:           8
        .value_kind:     global_buffer
      - .address_space:  global
        .offset:         8
        .size:           8
        .value_kind:     global_buffer
      - .offset:         16
        .size:           4
        .value_kind:     by_value
      - .offset:         20
        .size:           4
        .value_kind:     by_value
      - .offset:         24
        .size:           4
        .value_kind:     by_value
      - .actual_access:  read_only
        .address_space:  global
        .offset:         32
        .size:           8
        .value_kind:     global_buffer
      - .actual_access:  read_only
        .address_space:  global
        .offset:         40
        .size:           8
        .value_kind:     global_buffer
      - .actual_access:  write_only
        .address_space:  global
        .offset:         48
        .size:           8
        .value_kind:     global_buffer
      - .actual_access:  read_only
        .address_space:  global
        .offset:         56
        .size:           8
        .value_kind:     global_buffer
      - .actual_access:  read_only
        .address_space:  global
        .offset:         64
        .size:           8
        .value_kind:     global_buffer
    .group_segment_fixed_size: 131072
    .kernarg_segment_align: 8
    .kernarg_segment_size: 72
    .language:       OpenCL C
    .language_version:
      - 2
      - 0
    .max_flat_workgroup_size: 256
    .name:           _Z6gemm_kILi2ELi3ELi2EEvPKDF16_S1_iiiPKfS1_PDF16_PfS4_
    .private_segment_fixed_size: 0
    .sgpr_count:     54
    .sgpr_spill_count: 0
    .symbol:         _Z6gemm_kILi2ELi3ELi2EEvPKDF16_S1_iiiPKfS1_PDF16_PfS4_.kd
    .uniform_work_group_size: 1
    .uses_dynamic_stack: false
    .vgpr_count:     512
    .vgpr_spill_count: 0
    .wavefront_size: 64
